# H3 unit loop top: counted wait vmcnt(8) leaves the previous unit's eight epilogue stores in flight across the LDS refill and barrier (was a full drain); first entry keeps a full wait in the preheader
# speedup vs baseline: 1.0049x; 1.0049x over previous
.LBB0_760:
	s_andn2_b64 vcc, exec, s[2:3]
	s_cbranch_vccnz .LBB0_818
	v_readlane_b32 s2, v254, 1
	s_waitcnt vmcnt(0)
	v_mov_b32_e32 v1, v0
	v_readlane_b32 s3, v254, 2
	s_andn2_b64 vcc, exec, s[2:3]
	v_readfirstlane_b32 s2, v1
	s_movk_i32 s12, 0x2000
	s_cbranch_vccnz .LBB0_768
	s_lshl_b32 s34, s90, 11
	v_readlane_b32 s48, v251, 12
	s_lshl_b64 s[4:5], s[34:35], 2
	v_readlane_b32 s54, v251, 18
	v_readlane_b32 s55, v251, 19
	s_add_u32 s4, s54, s4
	s_addc_u32 s5, s55, s5
	s_ashr_i32 s6, s2, 8
	s_bfe_u32 s8, s2, 0x20006
	v_readlane_b32 s2, v254, 4
	s_mul_i32 s3, s6, 0x8800
	s_add_i32 s2, s6, s2
	s_add_i32 s7, s3, 0
	s_ashr_i32 s3, s2, 31
	v_and_b32_e32 v2, 63, v1
	s_lshl_b64 s[2:3], s[2:3], 15
	v_readlane_b32 s10, v253, 59
	v_lshl_or_b32 v37, s8, 6, v2
	v_readlane_b32 s11, v253, 60
	s_add_u32 s2, s10, s2
	s_addc_u32 s3, s11, s3
	v_lshlrev_b32_e32 v2, 4, v37
	v_lshl_add_u64 v[32:33], s[2:3], 0, v[2:3]
	v_add_co_u32_e32 v12, vcc, s12, v32
	global_load_dwordx4 v[4:7], v2, s[2:3] nt
	s_nop 0
	v_addc_co_u32_e32 v13, vcc, 0, v33, vcc
	s_movk_i32 s2, 0x4000
	v_add_co_u32_e32 v20, vcc, s2, v32
	s_movk_i32 s2, 0x6000
	s_nop 0
	v_addc_co_u32_e32 v21, vcc, 0, v33, vcc
	v_add_co_u32_e32 v28, vcc, s2, v32
	s_movk_i32 s2, 0x7000
	s_nop 0
	v_addc_co_u32_e32 v29, vcc, 0, v33, vcc
	v_add_co_u32_e32 v32, vcc, s2, v32
	global_load_dwordx4 v[8:11], v[12:13], off offset:-4096 nt
	s_nop 0
	global_load_dwordx4 v[12:15], v[12:13], off nt
	v_addc_co_u32_e32 v33, vcc, 0, v33, vcc
	global_load_dwordx4 v[16:19], v[20:21], off offset:-4096 nt
	s_nop 0
	global_load_dwordx4 v[20:23], v[20:21], off nt
	s_nop 0
	global_load_dwordx4 v[24:27], v[28:29], off offset:-4096 nt
	s_nop 0
	global_load_dwordx4 v[28:31], v[28:29], off nt
	v_lshlrev_b32_e32 v36, 4, v1
	global_load_dwordx4 v[32:35], v[32:33], off nt
	v_and_b32_e32 v36, 0xf0, v36
	v_add_u32_e32 v39, s7, v36
	v_lshrrev_b32_e32 v36, 2, v1
	v_readlane_b32 s2, v251, 63
	v_and_b32_e32 v38, 15, v1
	v_and_b32_e32 v40, 12, v36
	v_and_b32_e32 v36, 48, v1
	v_lshrrev_b32_e32 v1, 4, v37
	v_mov_b32_e32 v37, v3
	v_readlane_b32 s3, v252, 0
	v_lshl_add_u64 v[54:55], s[10:11], 0, v[2:3]
	v_lshlrev_b32_e32 v2, 1, v40
	v_lshl_add_u64 v[56:57], s[2:3], 0, v[36:37]
	v_readlane_b32 s2, v253, 45
	v_readlane_b32 s3, v253, 46
	v_lshl_or_b32 v52, s8, 4, v38
	v_add_u32_e32 v41, s7, v36
	v_lshl_add_u64 v[58:59], s[2:3], 0, v[2:3]
	v_readlane_b32 s2, v253, 63
	v_mul_u32_u24_e32 v1, 0x110, v1
	v_mul_u32_u24_e32 v38, 0x110, v38
	v_readlane_b32 s3, v254, 0
	v_lshlrev_b32_e32 v36, 2, v40
	v_lshl_add_u64 v[62:63], s[4:5], 0, v[36:37]
	v_lshl_add_u64 v[60:61], s[2:3], 0, v[2:3]
	v_lshl_add_u64 v[64:65], s[0:1], 0, v[2:3]
	v_add_u32_e32 v1, v39, v1
	v_add_u32_e32 v53, v41, v38
	v_readlane_b32 s9, v254, 3
	s_mov_b32 s10, s96
	v_readlane_b32 s49, v251, 13
	v_readlane_b32 s50, v251, 14
	v_readlane_b32 s51, v251, 15
	v_readlane_b32 s52, v251, 16
	v_readlane_b32 s53, v251, 17
	v_readlane_b32 s56, v251, 20
	v_readlane_b32 s57, v251, 21
	v_readlane_b32 s58, v251, 22
	v_readlane_b32 s59, v251, 23
	v_readlane_b32 s60, v251, 24
	v_readlane_b32 s61, v251, 25
	v_readlane_b32 s62, v251, 26
	v_readlane_b32 s63, v251, 27
	s_waitcnt vmcnt(0)
	s_branch .LBB0_764

.LBB0_764:
	s_waitcnt vmcnt(8)
	ds_write_b128 v1, v[4:7]
	ds_write_b128 v1, v[8:11] offset:4352
	ds_write_b128 v1, v[12:15] offset:8704
	ds_write_b128 v1, v[16:19] offset:13056
	ds_write_b128 v1, v[20:23] offset:17408
	ds_write_b128 v1, v[24:27] offset:21760
	ds_write_b128 v1, v[28:31] offset:26112
	ds_write_b128 v1, v[32:35] offset:30464
	s_waitcnt lgkmcnt(0)
	s_barrier
	s_add_i32 s7, s10, s20
	s_cmpk_gt_i32 s7, 0x3ff
	s_cselect_b64 s[4:5], -1, 0
	s_cmpk_lt_i32 s7, 0x400
	s_mov_b64 s[2:3], -1
	s_cbranch_scc1 .LBB0_766
	v_readlane_b32 s2, v254, 42
	s_add_i32 s8, s9, s2
	s_mov_b64 s[2:3], 0
